# fp8 GEMMs: post-K-loop MFMA-result hazard padding trimmed from 32 to 14 wait states (8-pass XDL -> VALU read needs 12)
# speedup vs baseline: 1.0060x; 1.0060x over previous
; #define PG8_BAR __builtin_amdgcn_s_barrier()
; template <class Epi, class Sched, bool ALIGN_EPI = false, bool SP2 = false, bool FP8 = false, bool GATHER = false>
; __device__ __forceinline__ void gemm_phase(PG8_LAS unsigned char* lds, const Gemm g, const Sched& S, const Epi& E) {
;     ...
;         if constexpr (FP8) asm volatile("s_nop 15\n\ts_nop 15" ::: "memory");
;         if constexpr (ALIGN_EPI) { if (wr == 0) PG8_BAR; }
.LBB0_883:
	s_nop 13
	s_and_b64 vcc, exec, s[26:27]
	s_cbranch_vccz .LBB0_885
	s_barrier

; #define PG8_BAR __builtin_amdgcn_s_barrier()
; template <class Epi, class Sched, bool ALIGN_EPI = false, bool SP2 = false, bool FP8 = false, bool GATHER = false>
; __device__ __forceinline__ void gemm_phase(PG8_LAS unsigned char* lds, const Gemm g, const Sched& S, const Epi& E) {
;     ...
;         if constexpr (FP8) asm volatile("s_nop 15\n\ts_nop 15" ::: "memory");
;         if constexpr (ALIGN_EPI) { if (wr == 0) PG8_BAR; }
.LBB0_962:
	s_nop 13
	s_and_b64 vcc, exec, s[20:21]
	s_cbranch_vccz .LBB0_964
	s_barrier

; #define PG8_BAR __builtin_amdgcn_s_barrier()
; template <class Epi, class Sched, bool ALIGN_EPI = false, bool SP2 = false, bool FP8 = false, bool GATHER = false>
; __device__ __forceinline__ void gemm_phase(PG8_LAS unsigned char* lds, const Gemm g, const Sched& S, const Epi& E) {
;     ...
;         if constexpr (FP8) asm volatile("s_nop 15\n\ts_nop 15" ::: "memory");
;         if constexpr (ALIGN_EPI) { if (wr == 0) PG8_BAR; }
.LBB0_1786:
	s_nop 13
	s_and_b64 vcc, exec, s[24:25]
	s_cbranch_vccz .LBB0_1788
	s_barrier

; #define PG8_BAR __builtin_amdgcn_s_barrier()
; template <class Epi, class Sched, bool ALIGN_EPI = false, bool SP2 = false, bool FP8 = false, bool GATHER = false>
; __device__ __forceinline__ void gemm_phase(PG8_LAS unsigned char* lds, const Gemm g, const Sched& S, const Epi& E) {
;     ...
;         if constexpr (FP8) asm volatile("s_nop 15\n\ts_nop 15" ::: "memory");
;         if constexpr (ALIGN_EPI) { if (wr == 0) PG8_BAR; }
.LBB0_1865:
	s_nop 13
	s_and_b64 vcc, exec, s[16:17]
	s_cbranch_vccz .LBB0_1867
	s_barrier
